# retention state buffer stored in the fragment order P3 reads it (4KB block permutation): P3 state loads and scan state stores become lane-contiguous
# speedup vs baseline: 1.0610x; 1.0098x over previous
; __device__ __forceinline__ unsigned pk2(float lo, float hi) { return f2bf(lo) | (f2bf(hi) << 16); }
; __device__ __forceinline__ void scan_task(const Frame& F, int task) {
;     ...
; #pragma unroll
;     for (int eb = 0; eb < 4; ++eb) { u32x2 w; w.x = pk2(st[eb][0], st[eb][1]); w.y = pk2(st[eb][2], st[eb][3]); st_u2(sp + (size_t)(NCH - 1) * HD * HD + eb * 16 * HD, w); }
.LBB0_482:
	s_or_b32 s0, s13, s9
	s_ashr_i32 s1, s0, 31
	s_lshl_b64 s[0:1], s[0:1], 12
	s_or_b32 s0, s0, s14
	v_bfe_u32 v2, v88, 16, 1
	v_mov_b32_e32 v1, s1
	v_mov_b32_e32 v0, s0
	v_readlane_b32 s0, v253, 46
	v_add3_u32 v2, v88, v2, s76
	v_bfe_u32 v3, v89, 16, 1
	v_lshlrev_b64 v[0:1], 8, v[0:1]
	v_readlane_b32 s1, v253, 47
	v_lshrrev_b32_e32 v2, 16, v2
	v_add3_u32 v3, v89, v3, s76
	v_lshl_add_u64 v[0:1], s[0:1], 0, v[0:1]
	s_lshl_b32 s96, s12, 5
	v_and_or_b32 v2, v3, s75, v2
	v_bfe_u32 v3, v90, 16, 1
	v_lshl_add_u64 v[0:1], v[0:1], 0, s[96:97]
	v_add3_u32 v3, v90, v3, s76
	v_bfe_u32 v4, v91, 16, 1
	v_lshl_add_u64 v[0:1], v[240:241], 0, v[0:1]
	v_lshrrev_b32_e32 v3, 16, v3
	v_add3_u32 v4, v91, v4, s76
	s_mov_b32 s0, 0xf9000
	v_and_or_b32 v3, v4, s75, v3
	v_add_co_u32_e32 v4, vcc, s0, v0
	v_bfe_u32 v6, v95, 16, 1
	s_nop 0
	v_addc_co_u32_e32 v5, vcc, 0, v1, vcc
	global_store_dwordx2 v[4:5], v[2:3], off offset:-4096
	v_bfe_u32 v2, v92, 16, 1
	v_add3_u32 v2, v92, v2, s76
	v_bfe_u32 v3, v93, 16, 1
	v_lshrrev_b32_e32 v2, 16, v2
	v_add3_u32 v3, v93, v3, s76
	v_and_or_b32 v2, v3, s75, v2
	v_bfe_u32 v3, v94, 16, 1
	v_add3_u32 v3, v94, v3, s76
	v_lshrrev_b32_e32 v3, 16, v3
	v_add3_u32 v6, v95, v6, s76
	v_and_or_b32 v3, v6, s75, v3
	global_store_dwordx2 v[4:5], v[2:3], off
	v_bfe_u32 v2, v84, 16, 1
	v_add3_u32 v2, v84, v2, s76
	v_bfe_u32 v3, v85, 16, 1
	v_lshrrev_b32_e32 v2, 16, v2
	v_add3_u32 v3, v85, v3, s76
	v_and_or_b32 v2, v3, s75, v2
	v_bfe_u32 v3, v86, 16, 1
	v_add3_u32 v3, v86, v3, s76
	v_bfe_u32 v4, v87, 16, 1
	v_lshrrev_b32_e32 v3, 16, v3
	v_add3_u32 v4, v87, v4, s76
	s_mov_b32 s0, 0xfa000
	v_and_or_b32 v3, v4, s75, v3
	v_add_co_u32_e32 v4, vcc, s0, v0
	v_readlane_b32 s0, v251, 18
	s_nop 0
	v_addc_co_u32_e32 v5, vcc, 0, v1, vcc
	global_store_dwordx2 v[4:5], v[2:3], off
	v_bfe_u32 v2, v80, 16, 1
	v_add3_u32 v2, v80, v2, s76
	v_bfe_u32 v3, v81, 16, 1
	v_lshrrev_b32_e32 v2, 16, v2
	v_add3_u32 v3, v81, v3, s76
	v_and_or_b32 v2, v3, s75, v2
	v_bfe_u32 v3, v82, 16, 1
	v_add3_u32 v3, v82, v3, s76
	v_bfe_u32 v4, v83, 16, 1
	v_lshrrev_b32_e32 v3, 16, v3
	v_add3_u32 v4, v83, v4, s76
	v_add_co_u32_e32 v0, vcc, 0xfb000, v0
	s_add_i32 s8, s8, s82
	s_add_i32 s3, s3, s67
	s_add_i32 s2, s2, s0
	v_and_or_b32 v3, v4, s75, v3
	v_addc_co_u32_e32 v1, vcc, 0, v1, vcc
	s_cmpk_gt_i32 s8, 0x3ff
	global_store_dwordx2 v[0:1], v[2:3], off
	s_cbranch_scc1 .LBB0_477

; #define LAS __attribute__((address_space(3)))
; __device__ __forceinline__ int lane_id() { return (int)__builtin_amdgcn_mbcnt_hi(~0u, __builtin_amdgcn_mbcnt_lo(~0u, 0u)); }
; __device__ __forceinline__ float fexp2(float x) { return __builtin_amdgcn_exp2f(x); }
; __device__ __forceinline__ void scan_task(const Frame& F, int task) {
;     int lane = lane_id(); asm volatile("" : "+v"(lane));
;     const int c = lane & 15, rq = lane >> 4;
;     const int eh = task & 1, db = (task >> 1) & 7, h = (task >> 4) & 7, b = task >> 7, bhh = b * NH + h;
;     const bf16* TOK = (const bf16*)(F.ws + WS_TOK); const bf16* SWP = (const bf16*)(F.ws + WS_SWP); bf16* ST = (bf16*)(F.ws + WS_ST);
;     const bf16* kg = TOK + (size_t)(b * S + (lane >> 1)) * TOKP + TK_KR + h * HD + db * 16 + (lane & 1) * 8;
;     const bf16* vrow = SWP + (size_t)(SW_VR + h * HD + eh * 64 + c) * SWPP + b * S + rq * 8;
;     bf16* sp = ST + ((size_t)bhh * NCH * HD + eh * 64 + c) * HD + db * 16 + rq * 4;
;     LAS unsigned char* kt = F.lds + RING_OFF + SC_OFF + F.wave * SC_WAVE_BYTES;
;     LAS unsigned char* kw = kt + (lane >> 1) * SC_PITCH + (lane & 1) * 16;
;     const LAS unsigned char* kr = kt + (rq * 8) * SC_PITCH + c * 2;
;     f32x4 st[4];
; #pragma unroll
;     for (int eb = 0; eb < 4; ++eb) st[eb] = (f32x4){0.f, 0.f, 0.f, 0.f};
;     const float lg = pg8::lg2gamma(h), cd = fexp2(64.f * lg);
;     float dec[16];
; #pragma unroll
;     for (int i = 0; i < 16; ++i) dec[i] = fexp2((float)(63 - ((i >> 3) * 32 + rq * 8 + (i & 7))) * lg);
;     ScanOps o0, o1, o2;
;     scan_load(o0, kg, vrow, 0); scan_load(o1, kg, vrow, 1);
.LBB0_504:
	s_lshr_b32 s0, s8, 4
	s_and_b32 s16, s0, 7
	s_lshl_b32 s0, s2, 1
	s_and_b32 s4, s0, 0xe0
	s_lshl_b32 s0, s16, 8
	v_mov_b32_e32 v184, s0
	s_ashr_i32 s0, s8, 7
	s_lshl_b32 s13, s0, 3
	s_lshl_b32 s0, s0, 11
	v_ashrrev_i32_e32 v6, 1, v0
	v_add_u32_e32 v92, s0, v6
	v_mov_b64_e32 v[2:3], s[62:63]
	s_movk_i32 s7, 0x2900
	v_mad_i64_i32 v[2:3], s[14:15], v92, s7, v[2:3]
	s_lshl_b32 s14, s8, 6
	s_lshl_b32 s1, s9, 7
	s_and_b32 s14, s14, 64
	v_and_b32_e32 v136, 15, v0
	s_or_b32 s1, s14, s1
	s_lshl_b32 s12, s8, 3
	v_or_b32_e32 v4, s1, v136
	s_waitcnt lgkmcnt(0)
	v_ashrrev_i32_e32 v1, 4, v0
	s_and_b32 s12, s12, 0x70
	v_mul_u32_u24_e32 v4, 0x4080, v4
	v_lshlrev_b32_e32 v0, 4, v0
	s_movk_i32 s15, 0x120
	s_lshl_b32 s96, s9, 8
	v_lshlrev_b32_e32 v84, 1, v4
	v_mov_b32_e32 v85, v185
	s_ashr_i32 s1, s0, 31
	v_lshlrev_b32_e32 v86, 3, v1
	v_lshlrev_b32_e32 v138, 2, v1
	v_and_b32_e32 v80, 16, v0
	v_mul_lo_u32 v7, v1, s15
	v_lshl_add_u64 v[0:1], v[2:3], 0, s[96:97]
	s_lshl_b32 s96, s12, 1
	v_lshl_add_u64 v[4:5], s[62:63], 0, v[84:85]
	v_ashrrev_i32_e32 v87, 31, v86
	v_lshl_add_u64 v[0:1], v[0:1], 0, s[96:97]
	v_mov_b32_e32 v81, v185
	s_lshl_b64 s[0:1], s[0:1], 1
	v_lshl_add_u64 v[16:17], v[0:1], 0, v[80:81]
	v_lshl_add_u64 v[0:1], v[4:5], 0, s[0:1]
	v_lshlrev_b64 v[88:89], 1, v[86:87]
	v_lshl_add_u64 v[18:19], v[0:1], 0, v[88:89]
	v_sub_u32_e32 v1, 63, v86
	v_cvt_f32_i32_e32 v1, v1
	v_readlane_b32 s6, v253, 48
	s_mov_b64 s[18:19], 0x1e840000
	s_waitcnt vmcnt(0)
	v_lshl_add_u64 v[44:45], v[18:19], 0, s[18:19]
	v_mov_b32_e32 v0, s6
	v_mad_u64_u32 v[90:91], s[18:19], v6, 36, v[0:1]
	v_mul_f32_e32 v0, v82, v1
	v_sub_u32_e32 v1, 62, v86
	v_cvt_f32_i32_e32 v1, v1
	v_sub_u32_e32 v2, 61, v86
	v_cvt_f32_i32_e32 v2, v2
	v_exp_f32_e32 v140, v0
	v_mul_f32_e32 v0, v82, v1
	v_sub_u32_e32 v1, 60, v86
	v_cvt_f32_i32_e32 v1, v1
	v_exp_f32_e32 v142, v0
	v_mul_f32_e32 v0, v82, v2
	s_mov_b32 s15, 0x12001000
	v_exp_f32_e32 v141, v0
	v_mul_f32_e32 v0, v82, v1
	v_add_co_u32_e32 v24, vcc, s15, v16
	v_exp_f32_e32 v143, v0
	v_sub_u32_e32 v0, 58, v86
	v_addc_co_u32_e32 v25, vcc, 0, v17, vcc
	s_mov_b32 s15, 0x12053000
	v_cvt_f32_i32_e32 v91, v0
	v_add_co_u32_e32 v0, vcc, s15, v16
	s_mov_b32 s15, 0x1e840000
	s_nop 0
	v_addc_co_u32_e32 v1, vcc, 0, v17, vcc
	v_add_co_u32_e32 v4, vcc, s15, v18
	s_mov_b32 s15, 0x1e8c1000
	s_nop 0
	v_addc_co_u32_e32 v5, vcc, 0, v19, vcc
	v_add_co_u32_e32 v60, vcc, s15, v18
	s_mov_b32 s15, 0x1e942000
	s_nop 0
	v_addc_co_u32_e32 v61, vcc, 0, v19, vcc
	v_add_co_u32_e32 v68, vcc, s15, v18
	s_mov_b32 s15, 0x1e9c3000
	s_nop 0
	v_addc_co_u32_e32 v69, vcc, 0, v19, vcc
	v_add_co_u32_e32 v76, vcc, s15, v18
	v_sub_u32_e32 v2, 59, v86
	s_nop 0
	v_addc_co_u32_e32 v77, vcc, 0, v19, vcc
	s_mov_b32 s15, 0x120a5000
	v_cvt_f32_i32_e32 v2, v2
	v_add_co_u32_e32 v18, vcc, s15, v16
	s_mov_b32 s15, 0x120f7000
	s_nop 0
	v_addc_co_u32_e32 v19, vcc, 0, v17, vcc
	v_add_co_u32_e32 v20, vcc, s15, v16
	v_add_u32_e32 v81, s6, v7
	s_nop 0
	v_addc_co_u32_e32 v21, vcc, 0, v17, vcc
	v_mul_f32_e32 v87, v82, v2
	global_load_dwordx4 v[0:3], v[0:1], off offset:2048
	s_nop 0
	global_load_dwordx4 v[4:7], v[4:5], off
	s_nop 0
	global_load_dwordx4 v[8:11], v[60:61], off
	s_waitcnt lgkmcnt(0)
	global_load_dwordx4 v[12:15], v[60:61], off offset:64
	global_load_dwordx4 v[28:31], v[68:69], off
	global_load_dwordx4 v[32:35], v[68:69], off offset:64
	global_load_dwordx4 v[48:51], v[76:77], off
	global_load_dwordx4 v[52:55], v[76:77], off offset:64
	s_nop 0
	global_load_dwordx4 v[16:19], v[18:19], off offset:2048
	s_nop 0
	global_load_dwordx4 v[20:23], v[20:21], off offset:2048
	s_nop 0
	global_load_dwordx4 v[40:43], v[44:45], off offset:64
	global_load_dwordx4 v[36:39], v[44:45], off offset:128
	s_nop 0
	global_load_dwordx4 v[24:27], v[24:25], off offset:2048
	s_nop 0
	global_load_dwordx4 v[44:47], v[44:45], off offset:192
	s_nop 0
	global_load_dwordx4 v[56:59], v[60:61], off offset:128
	s_nop 0
	global_load_dwordx4 v[60:63], v[60:61], off offset:192
	s_nop 0
	global_load_dwordx4 v[64:67], v[68:69], off offset:128
	s_nop 0
	global_load_dwordx4 v[68:71], v[68:69], off offset:192
	s_nop 0
	global_load_dwordx4 v[72:75], v[76:77], off offset:128
	s_nop 0
	global_load_dwordx4 v[76:79], v[76:77], off offset:192
	v_exp_f32_e32 v144, v87
	v_mul_f32_e32 v87, v82, v91
	v_sub_u32_e32 v91, 57, v86
	v_cvt_f32_i32_e32 v91, v91
	v_sub_u32_e32 v94, 56, v86
	v_cvt_f32_i32_e32 v94, v94
	v_exp_f32_e32 v146, v87
	v_mul_f32_e32 v87, v82, v91
	v_sub_u32_e32 v91, 31, v86
	v_cvt_f32_i32_e32 v91, v91
	v_exp_f32_e32 v145, v87
	v_mul_f32_e32 v87, v82, v94
	v_sub_u32_e32 v94, 30, v86
	v_cvt_f32_i32_e32 v94, v94
	v_exp_f32_e32 v147, v87
	v_mul_f32_e32 v87, v82, v91
	v_sub_u32_e32 v91, 29, v86
	v_cvt_f32_i32_e32 v91, v91
	v_exp_f32_e32 v148, v87
	v_mul_f32_e32 v87, v82, v94
	v_sub_u32_e32 v94, 28, v86
	v_cvt_f32_i32_e32 v94, v94
	v_exp_f32_e32 v150, v87
	v_mul_f32_e32 v87, v82, v91
	v_sub_u32_e32 v91, 27, v86
	v_cvt_f32_i32_e32 v91, v91
	v_exp_f32_e32 v149, v87
	v_mul_f32_e32 v87, v82, v94
	v_sub_u32_e32 v94, 26, v86
	v_cvt_f32_i32_e32 v94, v94
	v_exp_f32_e32 v151, v87
	v_mul_f32_e32 v87, v82, v91
	v_sub_u32_e32 v91, 25, v86
	v_sub_u32_e32 v86, 24, v86
	v_cvt_f32_i32_e32 v91, v91
	v_cvt_f32_i32_e32 v86, v86
	v_exp_f32_e32 v152, v87
	v_mul_f32_e32 v87, v82, v94
	v_mul_f32_e32 v83, 0x42800000, v82
	v_exp_f32_e32 v154, v87
	v_mul_f32_e32 v87, v82, v91
	v_mul_f32_e32 v82, v82, v86
	v_exp_f32_e32 v156, v83
	v_exp_f32_e32 v155, v82
	v_lshl_add_u64 v[82:83], s[0:1], 0, v[88:89]
	s_or_b32 s0, s13, s16
	s_ashr_i32 s1, s0, 31
	s_and_b32 s5, s3, 64
	s_lshl_b64 s[0:1], s[0:1], 12
	s_or_b32 s0, s0, s5
	v_exp_f32_e32 v153, v87
	v_lshl_add_u64 v[160:161], v[82:83], 0, v[84:85]
	v_mov_b32_e32 v82, s0
	v_mov_b32_e32 v83, s1
	v_lshlrev_b64 v[82:83], 8, v[82:83]
	v_ashrrev_i32_e32 v139, 31, v138
	v_lshlrev_b32_e32 v93, 1, v136
	v_lshl_or_b32 v82, s4, 4, v82
	v_mad_i64_i32 v[164:165], s[0:1], v92, s7, v[184:185]
	v_mov_b32_e32 v88, 0
	s_mov_b32 s15, 0
	v_mov_b32_e32 v158, v156
	v_mov_b32_e32 v159, v156
	v_and_b32_e32 v240, 8, v138
	v_and_b32_e32 v241, 4, v138
	v_lshlrev_b32_e32 v240, 5, v240
	v_lshl_or_b32 v240, v241, 1, v240
	v_lshl_or_b32 v240, v136, 4, v240
	v_mov_b32_e32 v241, 0
	v_lshl_add_u64 v[162:163], v[82:83], 0, v[240:241]
	v_or3_b32 v164, v164, s4, v80
	v_add_u32_e32 v137, v90, v80
	v_add_u32_e32 v168, v81, v93
	v_mov_b32_e32 v89, v88
	v_mov_b32_e32 v90, v88
	v_mov_b32_e32 v91, v88
	v_mov_b32_e32 v92, v88
	v_mov_b32_e32 v93, v88
	v_mov_b32_e32 v94, v88
	v_mov_b32_e32 v95, v88
	v_mov_b32_e32 v84, v88
	v_mov_b32_e32 v85, v88
	v_mov_b32_e32 v86, v88
	v_mov_b32_e32 v87, v88
	v_mov_b32_e32 v80, v88
	v_mov_b32_e32 v81, v88
	v_mov_b32_e32 v82, v88
	v_mov_b32_e32 v83, v88
	s_branch .LBB0_507

; __device__ __forceinline__ f32x4 mfma16(bf16x8 a, bf16x8 b, f32x4 c) { return __builtin_amdgcn_mfma_f32_16x16x32_bf16(a, b, c, 0, 0, 0); }
; __device__ __forceinline__ void ret_task(const Frame& F, int l, int task) {
;     ...
;     const bf16* sp = ST + (((size_t)bhh * NCH + n) * HD + c) * HD + rq * 8;
; #pragma unroll
;     for (int eb = 0; eb < 8; ++eb)
; #pragma unroll
;         for (int ks = 0; ks < 4; ++ks) { const bf16x8 sf = ld_b8(sp + eb * 16 * HD + ks * 32);
; #pragma unroll
;             for (int qb = 0; qb < 2; ++qb) acc[qb][eb] = mfma16(sf, Qf[qb][ks], acc[qb][eb]); }
.LBB0_655:
	s_bfe_u32 s1, s8, 0x50001
	s_ashr_i32 s0, s8, 9
	s_lshl_b32 s4, s0, 3
	s_lshl_b32 s0, s0, 11
	s_lshl_b32 s5, s1, 6
	v_and_b32_e32 v180, 15, v118
	s_or_b32 s0, s5, s0
	v_readlane_b32 s5, v251, 32
	v_ashrrev_i32_e32 v205, 4, v118
	s_or_b32 s4, s4, s9
	v_or_b32_e32 v209, s5, v180
	v_or_b32_e32 v196, s0, v209
	v_lshlrev_b32_e32 v202, 3, v205
	v_mov_b64_e32 v[160:161], s[80:81]
	s_movk_i32 s7, 0x2900
	s_ashr_i32 s5, s4, 31
	v_ashrrev_i32_e32 v203, 31, v202
	v_mad_i64_i32 v[198:199], s[12:13], v196, s7, v[160:161]
	s_lshl_b32 s96, s9, 8
	s_lshl_b64 s[4:5], s[4:5], 12
	s_lshl_b32 s1, s1, 7
	s_waitcnt lgkmcnt(0)
	v_lshl_add_u64 v[0:1], v[198:199], 0, s[96:97]
	v_lshlrev_b64 v[176:177], 1, v[202:203]
	s_or_b32 s1, s4, s1
	v_lshl_add_u64 v[8:9], v[0:1], 0, v[176:177]
	v_mov_b32_e32 v0, s1
	v_mov_b32_e32 v1, s5
	v_readlane_b32 s4, v253, 46
	v_lshlrev_b64 v[0:1], 8, v[0:1]
	v_readlane_b32 s5, v253, 47
	v_or_b32_e32 v194, 16, v196
	s_movk_i32 s6, 0x1000
	v_lshl_add_u64 v[0:1], s[4:5], 0, v[0:1]
	v_mad_i64_i32 v[200:201], s[4:5], v194, s7, v[160:161]
	v_add_co_u32_e32 v4, vcc, s6, v8
	s_mov_b64 s[4:5], 0x1000
	v_lshlrev_b32_e32 v2, 4, v180
	v_lshl_or_b32 v2, v205, 8, v2
	v_mov_b32_e32 v3, 0
	v_lshl_add_u64 v[36:37], v[0:1], 0, v[2:3]
	v_addc_co_u32_e32 v5, vcc, 0, v9, vcc
	v_lshl_add_u64 v[8:9], v[8:9], 0, s[4:5]
	global_load_dwordx4 v[0:3], v[36:37], off
	global_load_dwordx4 v[46:49], v[36:37], off offset:1024
	global_load_dwordx4 v[20:23], v[4:5], off
	global_load_dwordx4 v[52:55], v[8:9], off offset:64
	v_lshl_add_u64 v[4:5], v[200:201], 0, s[96:97]
	v_lshl_add_u64 v[12:13], v[4:5], 0, v[176:177]
	v_add_co_u32_e32 v4, vcc, s6, v12
	v_lshl_add_u64 v[80:81], v[12:13], 0, s[4:5]
	s_nop 0
	v_addc_co_u32_e32 v5, vcc, 0, v13, vcc
	global_load_dwordx4 v[24:27], v[4:5], off
	global_load_dwordx4 v[60:63], v[8:9], off offset:128
	global_load_dwordx4 v[56:59], v[80:81], off offset:64
	global_load_dwordx4 v[64:67], v[80:81], off offset:128
	s_movk_i32 s1, 0x2000
	v_add_co_u32_e32 v10, vcc, s1, v36
	s_movk_i32 s1, 0x4000
	s_nop 0
	v_addc_co_u32_e32 v11, vcc, 0, v37, vcc
	s_waitcnt lgkmcnt(0)
	global_load_dwordx4 v[14:17], v[10:11], off offset:-4096
	global_load_dwordx4 v[72:75], v[8:9], off offset:192
	s_waitcnt vmcnt(19)
	v_add_co_u32_e32 v50, vcc, s1, v36
	global_load_dwordx4 v[28:31], v[10:11], off
	s_nop 0
	v_addc_co_u32_e32 v51, vcc, 0, v37, vcc
	v_add_co_u32_e32 v84, vcc, s6, v36
	global_load_dwordx4 v[38:41], v[50:51], off offset:-4096
	global_load_dwordx4 v[112:115], v[50:51], off offset:2048
	v_addc_co_u32_e32 v85, vcc, 0, v37, vcc
	s_movk_i32 s1, 0x3000
	v_lshlrev_b32_e32 v119, 1, v118
	v_and_b32_e32 v118, 3, v118
	s_mov_b64 s[10:11], 0x1800
	s_lshl_b32 s9, s9, 7
	v_or_b32_e32 v228, 16, v209
	v_mov_b32_e32 v210, v202
	v_mov_b32_e32 v195, v202
	s_waitcnt vmcnt(10)
	v_mfma_f32_16x16x32_bf16 v[4:7], v[0:3], v[20:23], 0
	global_load_dwordx4 v[80:83], v[80:81], off offset:192
	s_waitcnt vmcnt(9)
	v_mfma_f32_16x16x32_bf16 v[0:3], v[0:3], v[24:27], 0
	v_mfma_f32_16x16x32_bf16 v[4:7], v[46:49], v[52:55], v[4:7]
	s_waitcnt vmcnt(7)
	v_mfma_f32_16x16x32_bf16 v[0:3], v[46:49], v[56:59], v[0:3]
	global_load_dwordx4 v[46:49], v[84:85], off offset:1024
	s_waitcnt vmcnt(6)
	v_mfma_f32_16x16x32_bf16 v[32:35], v[14:17], v[20:23], 0
	v_mfma_f32_16x16x32_bf16 v[14:17], v[14:17], v[24:27], 0
	s_waitcnt vmcnt(3)
	v_mfma_f32_16x16x32_bf16 v[68:71], v[38:41], v[20:23], 0
	s_waitcnt vmcnt(0)
	v_mfma_f32_16x16x32_bf16 v[12:15], v[46:49], v[56:59], v[14:17]
	s_nop 3
	global_load_dwordx4 v[16:19], v[10:11], off offset:1024
	v_mfma_f32_16x16x32_bf16 v[42:45], v[28:31], v[20:23], 0
	v_mfma_f32_16x16x32_bf16 v[28:31], v[28:31], v[24:27], 0
	v_mfma_f32_16x16x32_bf16 v[32:35], v[46:49], v[52:55], v[32:35]
	global_load_dwordx4 v[46:49], v[36:37], off offset:2048
	s_waitcnt vmcnt(1)
	v_mfma_f32_16x16x32_bf16 v[42:45], v[16:19], v[52:55], v[42:45]
	v_mfma_f32_16x16x32_bf16 v[16:19], v[16:19], v[56:59], v[28:31]
	s_nop 2
	global_load_dwordx4 v[28:31], v[84:85], off offset:2048
	s_waitcnt vmcnt(0)
	v_mfma_f32_16x16x32_bf16 v[76:79], v[28:31], v[64:67], v[12:15]
	s_nop 2
	global_load_dwordx4 v[12:15], v[36:37], off offset:3072
	v_mfma_f32_16x16x32_bf16 v[4:7], v[46:49], v[60:63], v[4:7]
	v_mfma_f32_16x16x32_bf16 v[0:3], v[46:49], v[64:67], v[0:3]
	v_mfma_f32_16x16x32_bf16 v[46:49], v[28:31], v[60:63], v[32:35]
	s_nop 2
	global_load_dwordx4 v[32:35], v[10:11], off offset:2048
	s_waitcnt vmcnt(1)
	v_mfma_f32_16x16x32_bf16 v[28:31], v[12:15], v[80:83], v[0:3]
	s_nop 2
	global_load_dwordx4 v[0:3], v[10:11], off offset:3072
	s_waitcnt vmcnt(1)
	v_mfma_f32_16x16x32_bf16 v[42:45], v[32:35], v[60:63], v[42:45]
	v_mfma_f32_16x16x32_bf16 v[16:19], v[32:35], v[64:67], v[16:19]
	v_mfma_f32_16x16x32_bf16 v[32:35], v[12:15], v[72:75], v[4:7]
	s_nop 2
	global_load_dwordx4 v[4:7], v[84:85], off offset:3072
	v_add_co_u32_e32 v84, vcc, s1, v36
	s_movk_i32 s1, 0x6000
	s_nop 0
	v_addc_co_u32_e32 v85, vcc, 0, v37, vcc
	s_waitcnt vmcnt(0)
	v_mfma_f32_16x16x32_bf16 v[12:15], v[4:7], v[72:75], v[46:49]
	s_nop 2
	global_load_dwordx4 v[46:49], v[84:85], off offset:1024
	v_add_co_u32_e32 v116, vcc, s1, v36
	v_mfma_f32_16x16x32_bf16 v[8:11], v[4:7], v[80:83], v[76:79]
	s_nop 0
	v_addc_co_u32_e32 v117, vcc, 0, v37, vcc
	s_movk_i32 s1, 0x5000
	v_mfma_f32_16x16x32_bf16 v[4:7], v[0:3], v[72:75], v[42:45]
	global_load_dwordx4 v[76:79], v[84:85], off offset:3072
	global_load_dwordx4 v[92:95], v[116:117], off
	global_load_dwordx4 v[88:91], v[116:117], off offset:1024
	global_load_dwordx4 v[42:45], v[84:85], off offset:2048
	v_mfma_f32_16x16x32_bf16 v[0:3], v[0:3], v[80:83], v[16:19]
	global_load_dwordx4 v[108:111], v[116:117], off offset:-4096
	v_mfma_f32_16x16x32_bf16 v[16:19], v[38:41], v[24:27], 0
	s_waitcnt vmcnt(5)
; __device__ __forceinline__ f32x4 mfma16(bf16x8 a, bf16x8 b, f32x4 c) { return __builtin_amdgcn_mfma_f32_16x16x32_bf16(a, b, c, 0, 0, 0); }
; __device__ __forceinline__ void ret_task(const Frame& F, int l, int task) {
;     ...
;     bf16x8 Qf[2][4], Kf[2][2][4];
; #pragma unroll
;     for (int qb = 0; qb < 2; ++qb)
; #pragma unroll
;         for (int ks = 0; ks < 4; ++ks) Qf[qb][ks] = ld_b8(TOK + (size_t)(tq0 + qb * 16 + c) * TOKP + TK_QR + h * HD + ks * 32 + rq * 8);
; #pragma unroll
;     for (int g = 0; g < 2; ++g)
; #pragma unroll
;         for (int ab = 0; ab < 2; ++ab) { const int key = 32 * g + (c >> 2) * 8 + 4 * ab + (c & 3);
; #pragma unroll
;             for (int ks = 0; ks < 4; ++ks) Kf[g][ab][ks] = ld_b8(TOK + (size_t)(tc0 + key) * TOKP + TK_KR + h * HD + rq * 8 + ks * 32); }
;     f32x4 acc[2][8];
; #pragma unroll
;     for (int qb = 0; qb < 2; ++qb)
; #pragma unroll
;         for (int eb = 0; eb < 8; ++eb) acc[qb][eb] = (f32x4){0.f, 0.f, 0.f, 0.f};
;     const bf16* sp = ST + (((size_t)bhh * NCH + n) * HD + c) * HD + rq * 8;
; #pragma unroll
;     for (int eb = 0; eb < 8; ++eb)
; #pragma unroll
;         for (int ks = 0; ks < 4; ++ks) { const bf16x8 sf = ld_b8(sp + eb * 16 * HD + ks * 32);
; #pragma unroll
;             for (int qb = 0; qb < 2; ++qb) acc[qb][eb] = mfma16(sf, Qf[qb][ks], acc[qb][eb]); }
;     bf16x8 Vf[8];
; #pragma unroll
;     for (int eb = 0; eb < 8; ++eb) Vf[eb] = ld_b8(SWP + (size_t)(SW_VR + h * HD + eb * 16 + c) * SWPP + tc0 + 8 * rq);
	v_mfma_f32_16x16x32_bf16 v[38:41], v[46:49], v[52:55], v[68:71]
	s_nop 2
	global_load_dwordx4 v[68:71], v[50:51], off offset:1024
	global_load_dwordx4 v[84:87], v[50:51], off
	v_mfma_f32_16x16x32_bf16 v[16:19], v[46:49], v[56:59], v[16:19]
	s_waitcnt vmcnt(3)
	v_mfma_f32_16x16x32_bf16 v[38:41], v[42:45], v[60:63], v[38:41]
	v_mfma_f32_16x16x32_bf16 v[42:45], v[42:45], v[64:67], v[16:19]
	v_mfma_f32_16x16x32_bf16 v[16:19], v[76:79], v[72:75], v[38:41]
	s_nop 5
	v_add_co_u32_e32 v38, vcc, s1, v36
	v_mfma_f32_16x16x32_bf16 v[40:43], v[76:79], v[80:83], v[42:45]
	s_nop 0
	v_addc_co_u32_e32 v39, vcc, 0, v37, vcc
	global_load_dwordx4 v[96:99], v[38:39], off offset:3072
	global_load_dwordx4 v[104:107], v[38:39], off offset:1024
	global_load_dwordx4 v[100:103], v[38:39], off offset:2048
	s_waitcnt vmcnt(3)
	v_mfma_f32_16x16x32_bf16 v[44:47], v[84:87], v[20:23], 0
	global_load_dwordx4 v[48:51], v[50:51], off offset:3072
	s_movk_i32 s1, 0x7000
	v_mfma_f32_16x16x32_bf16 v[76:79], v[84:87], v[24:27], 0
	v_mfma_f32_16x16x32_bf16 v[44:47], v[68:71], v[52:55], v[44:47]
	v_mfma_f32_16x16x32_bf16 v[68:71], v[68:71], v[56:59], v[76:79]
	s_nop 5
	global_load_dwordx4 v[76:79], v[116:117], off offset:2048
	global_load_dwordx4 v[84:87], v[116:117], off offset:3072
	v_add_co_u32_e32 v116, vcc, s1, v36
	v_mfma_f32_16x16x32_bf16 v[44:47], v[112:115], v[60:63], v[44:47]
	s_nop 0
	v_addc_co_u32_e32 v117, vcc, 0, v37, vcc
	global_load_dwordx4 v[36:39], v[116:117], off offset:1024
	v_mfma_f32_16x16x32_bf16 v[112:115], v[112:115], v[64:67], v[68:71]
	s_ashr_i32 s1, s0, 31
	s_nop 1
	global_load_dwordx4 v[68:71], v[116:117], off
	s_waitcnt vmcnt(4)
	v_mfma_f32_16x16x32_bf16 v[44:47], v[48:51], v[72:75], v[44:47]
	v_mfma_f32_16x16x32_bf16 v[48:51], v[48:51], v[80:83], v[112:115]
	s_nop 2
	v_and_b32_e32 v112, 24, v119
	v_mfma_f32_16x16x32_bf16 v[120:123], v[108:111], v[20:23], 0
	v_or3_b32 v162, v118, v112, s0
	v_mad_i64_i32 v[118:119], s[4:5], v162, s7, v[160:161]
	v_mfma_f32_16x16x32_bf16 v[124:127], v[108:111], v[24:27], 0
	global_load_dwordx4 v[112:115], v[116:117], off offset:2048
	v_lshl_add_u64 v[118:119], v[118:119], 0, s[96:97]
	v_lshl_add_u64 v[128:129], v[118:119], 0, v[176:177]
	v_mfma_f32_16x16x32_bf16 v[120:123], v[104:107], v[52:55], v[120:123]
	v_add_co_u32_e32 v108, vcc, s6, v128
	v_mfma_f32_16x16x32_bf16 v[104:107], v[104:107], v[56:59], v[124:127]
	s_nop 0
	v_addc_co_u32_e32 v109, vcc, 0, v129, vcc
	v_lshl_add_u64 v[128:129], v[128:129], 0, s[10:11]
	v_or_b32_e32 v124, 4, v162
	v_mad_i64_i32 v[124:125], s[4:5], v124, s7, v[160:161]
	v_lshl_add_u64 v[124:125], v[124:125], 0, s[96:97]
	global_load_dwordx4 v[108:111], v[108:109], off offset:2048
	v_lshl_add_u64 v[130:131], v[124:125], 0, v[176:177]
	global_load_dwordx4 v[124:127], v[128:129], off offset:64
	v_mfma_f32_16x16x32_bf16 v[120:123], v[100:103], v[60:63], v[120:123]
	global_load_dwordx4 v[116:119], v[116:117], off offset:3072
	v_mfma_f32_16x16x32_bf16 v[100:103], v[100:103], v[64:67], v[104:107]
	s_nop 2
	v_add_co_u32_e32 v104, vcc, s6, v130
	v_mfma_f32_16x16x32_bf16 v[144:147], v[96:99], v[72:75], v[120:123]
	s_nop 0
	v_addc_co_u32_e32 v105, vcc, 0, v131, vcc
	v_or_b32_e32 v106, s9, v180
	global_load_dwordx4 v[120:123], v[104:105], off offset:2048
	v_mfma_f32_16x16x32_bf16 v[148:151], v[96:99], v[80:83], v[100:103]
	global_load_dwordx4 v[168:171], v[128:129], off offset:128
	global_load_dwordx4 v[96:99], v[128:129], off offset:192
	v_mul_u32_u24_e32 v106, 0x4080, v106
	v_lshlrev_b32_e32 v184, 1, v106
	v_mfma_f32_16x16x32_bf16 v[100:103], v[92:95], v[20:23], 0
	v_or_b32_e32 v104, 32, v162
	v_lshl_add_u64 v[106:107], s[64:65], 0, v[184:185]
	v_mad_i64_i32 v[104:105], s[4:5], v104, s7, v[160:161]
	v_mfma_f32_16x16x32_bf16 v[92:95], v[92:95], v[24:27], 0
	v_lshl_add_u64 v[106:107], s[0:1], 1, v[106:107]
	v_lshl_add_u64 v[178:179], v[106:107], 0, v[176:177]
	s_mov_b32 s4, 0x23c7000
	v_mfma_f32_16x16x32_bf16 v[100:103], v[88:91], v[52:55], v[100:103]
	v_add_co_u32_e32 v106, vcc, s4, v178
	v_lshl_add_u64 v[128:129], v[130:131], 0, s[10:11]
	v_mfma_f32_16x16x32_bf16 v[88:91], v[88:91], v[56:59], v[92:95]
	v_addc_co_u32_e32 v107, vcc, 0, v179, vcc
	s_waitcnt vmcnt(10)
	v_mfma_f32_16x16x32_bf16 v[92:95], v[76:79], v[60:63], v[100:103]
	v_mfma_f32_16x16x32_bf16 v[100:103], v[76:79], v[64:67], v[88:91]
	global_load_dwordx4 v[76:79], v[106:107], off
	global_load_dwordx4 v[172:175], v[128:129], off offset:64
	s_nop 1
	v_lshl_add_u64 v[88:89], v[104:105], 0, s[96:97]
	s_waitcnt vmcnt(11)
	v_mfma_f32_16x16x32_bf16 v[152:155], v[84:87], v[72:75], v[92:95]
	v_lshl_add_u64 v[104:105], v[88:89], 0, v[176:177]
	global_load_dwordx4 v[88:91], v[128:129], off offset:192
	v_lshl_add_u64 v[106:107], v[104:105], 0, s[10:11]
	v_mfma_f32_16x16x32_bf16 v[156:159], v[84:87], v[80:83], v[100:103]
	global_load_dwordx4 v[84:87], v[128:129], off offset:128
	v_add_co_u32_e32 v104, vcc, s6, v104
	s_waitcnt vmcnt(11)
	v_mfma_f32_16x16x32_bf16 v[92:95], v[68:71], v[20:23], 0
	v_addc_co_u32_e32 v105, vcc, 0, v105, vcc
	global_load_dwordx4 v[132:135], v[106:107], off offset:64
	global_load_dwordx4 v[128:131], v[106:107], off offset:128
	v_mfma_f32_16x16x32_bf16 v[100:103], v[68:71], v[24:27], 0
	v_or_b32_e32 v68, 36, v162
	v_mad_i64_i32 v[68:69], s[4:5], v68, s7, v[160:161]
	v_mfma_f32_16x16x32_bf16 v[92:95], v[36:39], v[52:55], v[92:95]
	s_mov_b32 s4, 0x2040000
	v_add_co_u32_e32 v70, vcc, s4, v178
	v_mfma_f32_16x16x32_bf16 v[36:39], v[36:39], v[56:59], v[100:103]
	s_nop 0
	v_addc_co_u32_e32 v71, vcc, 0, v179, vcc
	s_mov_b32 s4, 0x20c1000
	s_waitcnt vmcnt(12)
; __device__ __forceinline__ f32x4 mfma16(bf16x8 a, bf16x8 b, f32x4 c) { return __builtin_amdgcn_mfma_f32_16x16x32_bf16(a, b, c, 0, 0, 0); }
; __device__ __forceinline__ float fexp2(float x) { return __builtin_amdgcn_exp2f(x); }
; __device__ __forceinline__ void ret_task(const Frame& F, int l, int task) {
;     ...
;     bf16x8 Vf[8];
; #pragma unroll
;     for (int eb = 0; eb < 8; ++eb) Vf[eb] = ld_b8(SWP + (size_t)(SW_VR + h * HD + eb * 16 + c) * SWPP + tc0 + 8 * rq);
; #pragma unroll
;     for (int qb = 0; qb < 2; ++qb) { const float f = fexp2((float)(qb2 * 32 + qb * 16 + c + 1) * lg);
; #pragma unroll
;         for (int eb = 0; eb < 8; ++eb) acc[qb][eb] *= f; }
;     f32x4 g4[8]; u32x2 gwq[2][8];
; #pragma unroll
;     for (int g = 0; g < 2; ++g) {
;         if (g <= qb2) {
;             f32x4 sa[2][2];
; #pragma unroll
;             for (int qb = 0; qb < 2; ++qb)
; #pragma unroll
;                 for (int ab = 0; ab < 2; ++ab) sa[qb][ab] = (f32x4){0.f, 0.f, 0.f, 0.f};
; #pragma unroll
;             for (int ab = 0; ab < 2; ++ab)
; #pragma unroll
;                 for (int ks = 0; ks < 4; ++ks)
; #pragma unroll
;                     for (int qb = 0; qb < 2; ++qb) sa[qb][ab] = mfma16(Kf[g][ab][ks], Qf[qb][ks], sa[qb][ab]);
;             bf16x8 Pf[2];
; #pragma unroll
;             for (int qb = 0; qb < 2; ++qb) {
;                 const int i = qb2 * 32 + qb * 16 + c;
; #pragma unroll
;                 for (int ab = 0; ab < 2; ++ab)
; #pragma unroll
;                     for (int e = 0; e < 4; ++e) { const int diff = i - (32 * g + 8 * rq + 4 * ab + e);
;                         sa[qb][ab][e] = diff >= 0 ? sa[qb][ab][e] * fexp2((float)diff * lg) : 0.f; }
	v_mfma_f32_16x16x32_bf16 v[36:39], v[112:115], v[64:67], v[36:39]
	global_load_dwordx4 v[140:143], v[104:105], off offset:2048
	global_load_dwordx4 v[136:139], v[106:107], off offset:192
	v_lshl_add_u64 v[68:69], v[68:69], 0, s[96:97]
	v_lshl_add_u64 v[68:69], v[68:69], 0, v[176:177]
	v_mfma_f32_16x16x32_bf16 v[100:103], v[112:115], v[60:63], v[92:95]
	s_nop 2
	global_load_dwordx4 v[92:95], v[70:71], off
	v_add_co_u32_e32 v70, vcc, s4, v178
	s_mov_b32 s4, 0x2142000
	s_nop 0
	v_addc_co_u32_e32 v71, vcc, 0, v179, vcc
	v_add_co_u32_e32 v104, vcc, s4, v178
	s_waitcnt vmcnt(12)
	v_mfma_f32_16x16x32_bf16 v[164:167], v[116:119], v[80:83], v[36:39]
	v_addc_co_u32_e32 v105, vcc, 0, v179, vcc
	s_mov_b32 s4, 0x21c3000
	v_mfma_f32_16x16x32_bf16 v[36:39], v[108:111], v[20:23], 0
	v_mfma_f32_16x16x32_bf16 v[108:111], v[108:111], v[24:27], 0
	v_mfma_f32_16x16x32_bf16 v[160:163], v[116:119], v[72:75], v[100:103]
	s_nop 2
	global_load_dwordx4 v[100:103], v[70:71], off
	s_nop 0
	global_load_dwordx4 v[104:107], v[104:105], off
	v_add_co_u32_e32 v70, vcc, s4, v178
	s_mov_b32 s4, 0x2244000
	s_nop 0
	v_addc_co_u32_e32 v71, vcc, 0, v179, vcc
	v_add_co_u32_e32 v116, vcc, s4, v178
	v_readlane_b32 s4, v251, 33
	s_nop 0
	v_addc_co_u32_e32 v117, vcc, 0, v179, vcc
	v_mfma_f32_16x16x32_bf16 v[36:39], v[124:127], v[52:55], v[36:39]
	global_load_dwordx4 v[112:115], v[70:71], off
	s_nop 0
	global_load_dwordx4 v[116:119], v[116:117], off
	v_add_u32_e32 v70, s4, v180
	v_cvt_f32_ubyte0_e32 v71, v70
	v_mfma_f32_16x16x32_bf16 v[108:111], v[124:127], v[56:59], v[108:111]
	v_add_u32_e32 v70, 16, v70
	v_cvt_f32_ubyte0_e32 v70, v70
	v_or_b32_e32 v126, 2, v202
	v_mul_f32_e32 v71, v197, v71
	v_mul_f32_e32 v70, v197, v70
	s_waitcnt vmcnt(14)
	v_mfma_f32_16x16x32_bf16 v[36:39], v[168:171], v[60:63], v[36:39]
	v_exp_f32_e32 v204, v71
	v_exp_f32_e32 v206, v70
	v_or_b32_e32 v127, 3, v202
	v_mfma_f32_16x16x32_bf16 v[108:111], v[168:171], v[64:67], v[108:111]
	v_sub_u32_e32 v169, v209, v202
	v_sub_u32_e32 v170, v209, v126
	v_cvt_f32_u32_e32 v70, v169
	v_cvt_f32_u32_e32 v71, v170
	s_waitcnt vmcnt(13)
	v_mfma_f32_16x16x32_bf16 v[36:39], v[96:99], v[72:75], v[36:39]
	v_or_b32_e32 v168, 1, v202
	v_mul_f32_e32 v70, v197, v70
	v_mul_f32_e32 v71, v197, v71
	v_exp_f32_e32 v70, v70
	v_exp_f32_e32 v71, v71
	v_mfma_f32_16x16x32_bf16 v[96:99], v[96:99], v[80:83], v[108:111]
	s_nop 1
	v_mov_b32_e32 v124, v36
	v_mov_b32_e32 v125, v38
	v_pk_mul_f32 v[70:71], v[70:71], v[124:125]
	v_mfma_f32_16x16x32_bf16 v[108:111], v[120:123], v[20:23], 0
	v_cmp_lt_i32_e32 vcc, -1, v170
	v_sub_u32_e32 v125, v209, v127
	v_cvt_f32_u32_e32 v38, v125
	v_mfma_f32_16x16x32_bf16 v[120:123], v[120:123], v[24:27], 0
	v_cndmask_b32_e32 v124, 0, v71, vcc
	v_sub_u32_e32 v71, v209, v168
	v_cvt_f32_u32_e32 v36, v71
	s_waitcnt vmcnt(11)
	v_mfma_f32_16x16x32_bf16 v[108:111], v[172:175], v[52:55], v[108:111]
	v_cmp_lt_i32_e32 vcc, -1, v169
	v_pk_mul_f32 v[14:15], v[204:205], v[14:15] op_sel_hi:[0,1]
	v_mul_f32_e32 v36, v197, v36
	v_mfma_f32_16x16x32_bf16 v[120:123], v[172:175], v[56:59], v[120:123]
	v_mul_f32_e64 v12, v204, v12
	v_mul_f32_e64 v13, v204, v13
	s_mov_b32 s4, 0x22c5000
	v_pk_mul_f32 v[6:7], v[204:205], v[6:7] op_sel_hi:[0,1]
	s_waitcnt vmcnt(9)
	v_mfma_f32_16x16x32_bf16 v[108:111], v[84:87], v[60:63], v[108:111]
	v_mul_f32_e64 v4, v204, v4
	v_mul_f32_e64 v5, v204, v5
	v_pk_mul_f32 v[30:31], v[206:207], v[30:31] op_sel_hi:[0,1]
	v_pk_mul_f32 v[28:29], v[206:207], v[28:29] op_sel_hi:[0,1]
	v_mfma_f32_16x16x32_bf16 v[84:87], v[84:87], v[64:67], v[120:123]
	v_mul_f32_e64 v2, v206, v2
	v_mul_f32_e64 v3, v206, v3
	v_pk_mul_f32 v[0:1], v[206:207], v[0:1] op_sel_hi:[0,1]
	v_pk_mul_f32 v[34:35], v[204:205], v[34:35] op_sel_hi:[0,1]
	v_exp_f32_e32 v120, v36
	v_mul_f32_e32 v36, v197, v38
	v_exp_f32_e32 v121, v36
	v_mov_b32_e32 v38, v37
	v_cndmask_b32_e32 v122, 0, v70, vcc
	v_cmp_lt_i32_e32 vcc, -1, v71
	v_pk_mul_f32 v[36:37], v[120:121], v[38:39]
	v_mfma_f32_16x16x32_bf16 v[108:111], v[88:91], v[72:75], v[108:111]
	v_sub_u32_e32 v39, v228, v126
	v_cvt_f32_u32_e32 v70, v39
	v_sub_u32_e32 v120, v228, v127
	v_mfma_f32_16x16x32_bf16 v[84:87], v[88:91], v[80:83], v[84:87]
	v_cndmask_b32_e32 v88, 0, v36, vcc
	v_cmp_lt_i32_e32 vcc, -1, v125
	v_sub_u32_e32 v91, v228, v168
	v_sub_u32_e32 v89, v228, v202
	v_cndmask_b32_e32 v90, 0, v37, vcc
	v_cvt_f32_u32_e32 v37, v91
	v_cvt_f32_u32_e32 v36, v89
	v_mov_b32_e32 v71, v98
	v_cmp_lt_i32_e32 vcc, -1, v39
	v_mul_f32_e32 v37, v197, v37
	v_mul_f32_e32 v36, v197, v36
	v_exp_f32_e32 v38, v37
	v_mul_f32_e32 v37, v197, v70
	v_exp_f32_e32 v36, v36
	v_exp_f32_e32 v37, v37
	v_mov_b32_e32 v70, v96
	v_cvt_f32_u32_e32 v96, v120
	v_mov_b32_e32 v98, v97
	v_pk_mul_f32 v[36:37], v[36:37], v[70:71]
	v_or_b32_e32 v123, 5, v202
	v_cndmask_b32_e32 v121, 0, v37, vcc
	v_mul_f32_e32 v37, v197, v96
	v_exp_f32_e32 v39, v37
	v_cmp_lt_i32_e32 vcc, -1, v89
	v_or_b32_e32 v97, 6, v202
	v_sub_u32_e32 v125, v209, v123
	v_cndmask_b32_e32 v89, 0, v36, vcc
	v_pk_mul_f32 v[36:37], v[38:39], v[98:99]
	v_cmp_lt_i32_e32 vcc, -1, v91
	v_or_b32_e32 v98, 4, v202
	v_sub_u32_e32 v99, v209, v98
	v_cndmask_b32_e32 v91, 0, v36, vcc
	v_cmp_lt_i32_e32 vcc, -1, v120
	v_sub_u32_e32 v39, v209, v97
	v_cvt_f32_u32_e32 v36, v99
	v_cndmask_b32_e32 v96, 0, v37, vcc
	v_cvt_f32_u32_e32 v37, v125
	v_cvt_f32_u32_e32 v70, v39
	v_or_b32_e32 v120, 7, v202
	v_mul_f32_e32 v36, v197, v36
	v_mul_f32_e32 v37, v197, v37
	v_exp_f32_e32 v38, v37
	v_mul_f32_e32 v37, v197, v70
	v_exp_f32_e32 v36, v36
	v_sub_u32_e32 v126, v209, v120
	v_exp_f32_e32 v37, v37
	v_mov_b32_e32 v70, v108
	v_cvt_f32_u32_e32 v108, v126
	v_mov_b32_e32 v71, v110
	v_pk_mul_f32 v[36:37], v[36:37], v[70:71]
; __device__ __forceinline__ f32x4 mfma16(bf16x8 a, bf16x8 b, f32x4 c) { return __builtin_amdgcn_mfma_f32_16x16x32_bf16(a, b, c, 0, 0, 0); }
; __device__ __forceinline__ float fexp2(float x) { return __builtin_amdgcn_exp2f(x); }
; __device__ __forceinline__ void ret_task(const Frame& F, int l, int task) {
;     ...
;     for (int qb = 0; qb < 2; ++qb) { const float f = fexp2((float)(qb2 * 32 + qb * 16 + c + 1) * lg);
; #pragma unroll
;         for (int eb = 0; eb < 8; ++eb) acc[qb][eb] *= f; }
;     f32x4 g4[8]; u32x2 gwq[2][8];
; #pragma unroll
;     for (int g = 0; g < 2; ++g) {
;         if (g <= qb2) {
;             f32x4 sa[2][2];
; #pragma unroll
;             for (int qb = 0; qb < 2; ++qb)
; #pragma unroll
;                 for (int ab = 0; ab < 2; ++ab) sa[qb][ab] = (f32x4){0.f, 0.f, 0.f, 0.f};
; #pragma unroll
;             for (int ab = 0; ab < 2; ++ab)
; #pragma unroll
;                 for (int ks = 0; ks < 4; ++ks)
; #pragma unroll
;                     for (int qb = 0; qb < 2; ++qb) sa[qb][ab] = mfma16(Kf[g][ab][ks], Qf[qb][ks], sa[qb][ab]);
;             bf16x8 Pf[2];
; #pragma unroll
;             for (int qb = 0; qb < 2; ++qb) {
;                 const int i = qb2 * 32 + qb * 16 + c;
; #pragma unroll
;                 for (int ab = 0; ab < 2; ++ab)
; #pragma unroll
;                     for (int e = 0; e < 4; ++e) { const int diff = i - (32 * g + 8 * rq + 4 * ab + e);
;                         sa[qb][ab][e] = diff >= 0 ? sa[qb][ab][e] * fexp2((float)diff * lg) : 0.f; }
;                 Pf[qb] = pack8(sa[qb][0], sa[qb][1]);
;             }
; #pragma unroll
;             for (int eb = 0; eb < 8; ++eb)
; #pragma unroll
;                 for (int qb = 0; qb < 2; ++qb) acc[qb][eb] = mfma16(Vf[eb], Pf[qb], acc[qb][eb]);
	v_cmp_lt_i32_e32 vcc, -1, v39
	v_mov_b32_e32 v110, v109
	v_sub_u32_e32 v98, v228, v98
	v_cndmask_b32_e32 v127, 0, v37, vcc
	v_mul_f32_e32 v37, v197, v108
	v_exp_f32_e32 v39, v37
	v_cmp_lt_i32_e32 vcc, -1, v99
	v_mov_b32_e32 v71, v86
	v_mov_b32_e32 v86, v85
	v_cndmask_b32_e32 v99, 0, v36, vcc
	v_pk_mul_f32 v[36:37], v[38:39], v[110:111]
	v_cmp_lt_i32_e32 vcc, -1, v125
	v_sub_u32_e32 v39, v228, v97
	v_sub_u32_e32 v97, v228, v123
	v_cndmask_b32_e32 v108, 0, v36, vcc
	v_cmp_lt_i32_e32 vcc, -1, v126
	v_cvt_f32_u32_e32 v36, v98
	v_cvt_f32_u32_e32 v70, v39
	v_cndmask_b32_e32 v109, 0, v37, vcc
	v_cvt_f32_u32_e32 v37, v97
	v_mul_f32_e32 v36, v197, v36
	v_exp_f32_e32 v36, v36
	v_sub_u32_e32 v110, v228, v120
	v_mul_f32_e32 v37, v197, v37
	v_exp_f32_e32 v38, v37
	v_mul_f32_e32 v37, v197, v70
	v_exp_f32_e32 v37, v37
	v_mov_b32_e32 v70, v84
	v_cvt_f32_u32_e32 v84, v110
	v_cmp_lt_i32_e32 vcc, -1, v39
	v_pk_mul_f32 v[36:37], v[36:37], v[70:71]
	v_bfe_u32 v85, v108, 16, 1
	v_cndmask_b32_e32 v70, 0, v37, vcc
	v_mul_f32_e32 v37, v197, v84
	v_exp_f32_e32 v39, v37
	v_cmp_lt_i32_e32 vcc, -1, v98
	v_bfe_u32 v84, v109, 16, 1
	v_add3_u32 v85, v108, v85, s76
	v_cndmask_b32_e32 v71, 0, v36, vcc
	v_pk_mul_f32 v[36:37], v[38:39], v[86:87]
	v_bfe_u32 v38, v90, 16, 1
	v_bfe_u32 v39, v88, 16, 1
	v_add3_u32 v39, v88, v39, s76
	v_add3_u32 v38, v90, v38, s76
	v_bfe_u32 v86, v99, 16, 1
	v_bfe_u32 v87, v127, 16, 1
	v_bfe_u32 v88, v122, 16, 1
	v_bfe_u32 v90, v124, 16, 1
	v_cmp_lt_i32_e32 vcc, -1, v97
	v_add3_u32 v90, v124, v90, s76
	v_add3_u32 v88, v122, v88, s76
	v_add3_u32 v87, v127, v87, s76
	v_add3_u32 v86, v99, v86, s76
	v_cndmask_b32_e32 v36, 0, v36, vcc
	v_cmp_lt_i32_e32 vcc, -1, v110
	v_add3_u32 v84, v109, v84, s76
	v_lshrrev_b32_e32 v86, 16, v86
	v_lshrrev_b32_e32 v87, 16, v87
	v_lshrrev_b32_e32 v88, 16, v88
	v_lshrrev_b32_e32 v90, 16, v90
	v_cndmask_b32_e32 v37, 0, v37, vcc
	v_and_or_b32 v231, v38, s75, v90
	v_and_or_b32 v230, v39, s75, v88
	v_and_or_b32 v233, v84, s75, v87
	v_and_or_b32 v232, v85, s75, v86
	v_bfe_u32 v84, v96, 16, 1
	v_bfe_u32 v38, v37, 16, 1
	v_add3_u32 v84, v96, v84, s76
	s_waitcnt vmcnt(3)
	v_mfma_f32_16x16x32_bf16 v[96:99], v[100:103], v[230:233], v[12:15]
	v_bfe_u32 v39, v36, 16, 1
	v_bfe_u32 v85, v91, 16, 1
	v_add3_u32 v37, v37, v38, s76
	v_add_co_u32_e32 v12, vcc, s4, v178
	v_bfe_u32 v38, v89, 16, 1
	s_nop 0
	v_addc_co_u32_e32 v13, vcc, 0, v179, vcc
	s_mov_b32 s4, 0x2346000
	v_add3_u32 v85, v91, v85, s76
	v_add3_u32 v36, v36, v39, s76
	v_bfe_u32 v39, v121, 16, 1
	v_add3_u32 v38, v89, v38, s76
	s_waitcnt vmcnt(2)
	v_mfma_f32_16x16x32_bf16 v[88:91], v[104:107], v[230:233], v[4:7]
	v_add3_u32 v39, v121, v39, s76
	global_load_dwordx4 v[120:123], v[12:13], off
	v_bfe_u32 v86, v71, 16, 1
	v_add_co_u32_e32 v4, vcc, s4, v178
	v_bfe_u32 v87, v70, 16, 1
	s_nop 0
	v_addc_co_u32_e32 v5, vcc, 0, v179, vcc
	global_load_dwordx4 v[124:127], v[4:5], off
	v_add_co_u32_e32 v6, vcc, s6, v68
	v_lshl_add_u64 v[4:5], v[68:69], 0, s[10:11]
	s_nop 0
	v_addc_co_u32_e32 v7, vcc, 0, v69, vcc
	global_load_dwordx4 v[172:175], v[4:5], off offset:64
	global_load_dwordx4 v[168:171], v[4:5], off offset:128
	global_load_dwordx4 v[180:183], v[6:7], off offset:2048
	global_load_dwordx4 v[176:179], v[4:5], off offset:192
	v_add3_u32 v70, v70, v87, s76
	v_add3_u32 v71, v71, v86, s76
	v_lshrrev_b32_e32 v38, 16, v38
	v_lshrrev_b32_e32 v39, 16, v39
	v_lshrrev_b32_e32 v71, 16, v71
	v_lshrrev_b32_e32 v70, 16, v70
	v_and_or_b32 v237, v37, s75, v70
	v_and_or_b32 v236, v36, s75, v71
	v_and_or_b32 v235, v84, s75, v39
	v_and_or_b32 v234, v85, s75, v38
	v_readlane_b32 s4, v251, 34
	v_pk_mul_f32 v[32:33], v[204:205], v[32:33] op_sel_hi:[0,1]
	v_mfma_f32_16x16x32_bf16 v[36:39], v[92:95], v[234:237], v[28:31]
	v_mul_f32_e64 v10, v206, v10
	v_mul_f32_e64 v11, v206, v11
	v_pk_mul_f32 v[8:9], v[206:207], v[8:9] op_sel_hi:[0,1]
	v_pk_mul_f32 v[6:7], v[206:207], v[150:151] op_sel_hi:[0,1]
	v_mfma_f32_16x16x32_bf16 v[28:31], v[104:107], v[234:237], v[0:3]
	v_mul_f32_e64 v4, v206, v148
	v_mul_f32_e64 v5, v206, v149
	v_readlane_b32 s5, v251, 35
	s_andn2_b64 vcc, exec, s[4:5]
	v_pk_mul_f32 v[2:3], v[204:205], v[18:19] op_sel_hi:[0,1]
	v_pk_mul_f32 v[0:1], v[204:205], v[16:17] op_sel_hi:[0,1]
	v_mfma_f32_16x16x32_bf16 v[108:111], v[92:95], v[230:233], v[32:35]
	s_waitcnt vmcnt(7)
	v_mfma_f32_16x16x32_bf16 v[84:87], v[112:115], v[230:233], v[0:3]
	s_nop 2
	v_mul_f32_e64 v2, v206, v42
	v_mul_f32_e64 v3, v206, v43
	v_pk_mul_f32 v[0:1], v[206:207], v[40:41] op_sel_hi:[0,1]
	v_mfma_f32_16x16x32_bf16 v[32:35], v[100:103], v[234:237], v[8:11]
	v_mul_f32_e64 v42, v204, v162
	v_mul_f32_e64 v43, v204, v163
	v_pk_mul_f32 v[40:41], v[204:205], v[160:161] op_sel_hi:[0,1]
	v_mfma_f32_16x16x32_bf16 v[16:19], v[112:115], v[234:237], v[0:3]
	s_nop 2
	v_mul_f32_e64 v2, v204, v46
	v_mul_f32_e64 v3, v204, v47
	v_pk_mul_f32 v[0:1], v[204:205], v[44:45] op_sel_hi:[0,1]
	s_waitcnt vmcnt(5)
	v_mfma_f32_16x16x32_bf16 v[8:11], v[120:123], v[234:237], v[4:7]
	v_mfma_f32_16x16x32_bf16 v[68:71], v[116:119], v[230:233], v[0:3]
	s_nop 2
	v_mul_f32_e64 v2, v206, v50
	v_mul_f32_e64 v3, v206, v51
	v_pk_mul_f32 v[0:1], v[206:207], v[48:49] op_sel_hi:[0,1]
	v_mfma_f32_16x16x32_bf16 v[40:43], v[76:79], v[230:233], v[40:43]
	s_nop 0
	v_mfma_f32_16x16x32_bf16 v[12:15], v[116:119], v[234:237], v[0:3]
	s_nop 2
	v_mul_f32_e64 v2, v204, v146
	v_mul_f32_e64 v3, v204, v147
	v_pk_mul_f32 v[0:1], v[204:205], v[144:145] op_sel_hi:[0,1]
	v_pk_mul_f32 v[146:147], v[206:207], v[166:167] op_sel_hi:[0,1]
	v_pk_mul_f32 v[144:145], v[206:207], v[164:165] op_sel_hi:[0,1]
	v_mfma_f32_16x16x32_bf16 v[48:51], v[120:123], v[230:233], v[0:3]
	s_nop 2
	v_mul_f32_e64 v2, v204, v154
	v_mul_f32_e64 v3, v204, v155
	v_pk_mul_f32 v[0:1], v[204:205], v[152:153] op_sel_hi:[0,1]
	s_waitcnt vmcnt(4)
	s_nop 0
	v_mfma_f32_16x16x32_bf16 v[44:47], v[124:127], v[230:233], v[0:3]
	s_nop 2
	v_mul_f32_e64 v2, v206, v158
	v_mul_f32_e64 v3, v206, v159
	v_pk_mul_f32 v[0:1], v[206:207], v[156:157] op_sel_hi:[0,1]
	s_nop 1
	v_mfma_f32_16x16x32_bf16 v[4:7], v[124:127], v[234:237], v[0:3]
	s_nop 2
	v_cndmask_b32_e64 v0, 0, 1, s[4:5]
	v_cmp_ne_u32_e64 s[34:35], 1, v0
	v_mfma_f32_16x16x32_bf16 v[0:3], v[76:79], v[234:237], v[144:147]
	s_cbranch_vccnz .LBB0_657
; __device__ __forceinline__ void ret_task(const Frame& F, int l, int task) {
;     ...
;             if (qb2) {
; #pragma unroll
;                 for (int eb = 0; eb < 8; ++eb) Vf[eb] = ld_b8(SWP + (size_t)(SW_VR + h * HD + eb * 16 + c) * SWPP + tc0 + 32 + 8 * rq);
;             }
	s_lshl_b64 s[0:1], s[0:1], 1
	s_add_u32 s0, s64, s0
	s_addc_u32 s1, s65, s1
	v_lshl_add_u64 v[76:77], s[0:1], 0, v[184:185]
	v_lshl_add_u64 v[76:77], v[202:203], 1, v[76:77]
	v_add_co_u32_e32 v78, vcc, 0x2040000, v76
	s_nop 1
	v_addc_co_u32_e32 v79, vcc, 0, v77, vcc
	v_add_co_u32_e32 v100, vcc, 0x20c1000, v76
	s_nop 1
	v_addc_co_u32_e32 v101, vcc, 0, v77, vcc
	global_load_dwordx4 v[92:95], v[78:79], off offset:64
	s_nop 0
	global_load_dwordx4 v[100:103], v[100:101], off offset:64
	v_add_co_u32_e32 v78, vcc, 0x2142000, v76
	s_nop 1
	v_addc_co_u32_e32 v79, vcc, 0, v77, vcc
	v_add_co_u32_e32 v112, vcc, 0x21c3000, v76
	s_nop 1
	v_addc_co_u32_e32 v113, vcc, 0, v77, vcc
	global_load_dwordx4 v[104:107], v[78:79], off offset:64
	s_nop 0
	global_load_dwordx4 v[112:115], v[112:113], off offset:64
	v_add_co_u32_e32 v78, vcc, 0x2244000, v76
	s_nop 1
	v_addc_co_u32_e32 v79, vcc, 0, v77, vcc
	v_add_co_u32_e32 v120, vcc, 0x22c5000, v76
	s_nop 1
	v_addc_co_u32_e32 v121, vcc, 0, v77, vcc
	global_load_dwordx4 v[116:119], v[78:79], off offset:64
	s_nop 0
	global_load_dwordx4 v[120:123], v[120:121], off offset:64
	v_add_co_u32_e32 v78, vcc, 0x2346000, v76
	s_nop 1
	v_addc_co_u32_e32 v79, vcc, 0, v77, vcc
	v_add_co_u32_e32 v76, vcc, 0x23c7000, v76
	s_nop 1
	v_addc_co_u32_e32 v77, vcc, 0, v77, vcc
	global_load_dwordx4 v[124:127], v[78:79], off offset:64
	s_nop 0
	global_load_dwordx4 v[76:79], v[76:77], off offset:64
